# P0 row passes: eight start groups 1.2 us apart instead of four 2.4 us apart
# baseline (speedup 1.0000x reference)
; #define LAS __attribute__((address_space(3)))
; __device__ __forceinline__ void phase_p0(Frame& F, const Ptrs& P) {
;     ...
;     __syncthreads();
;     { LAS float* wl = (LAS float*)F.lds;
;       for (int k = F.tid; k < DM; k += NWAVES * 64) { const float gk = P.norm_mix[k]; const float* wp = P.ev_w_in + (size_t)k * EVEN_IN + 1536; LAS float* d = wl + 8 * k + 4 * (k >> 3);
;           *(LAS f32x4*)d = *(const f32x4*)wp * gk; *(LAS f32x4*)(d + 4) = *(const f32x4*)(wp + 4) * gk; }
;       __syncthreads();
; #pragma unroll
;       for (int j = 0; j < 16; ++j) { const int k = (j < 8 ? 0 : 512) + 8 * lane + (j & 7); const LAS float* s = wl + 8 * k + 4 * (k >> 3); wf[j][0] = *(const LAS f32x4*)s; wf[j][1] = *(const LAS f32x4*)(s + 4); } }
;     float* LF = (float*)(ws + WS_LF); const float bfl = P.ev_b_f[lane & 7];
;     for (int r0 = gw * 4; r0 < TOK; r0 += NGW * 4) {
;         f32x4 a[4][4];
; #pragma unroll
;         for (int q = 0; q < 4; ++q) { const float* s = P.x + (size_t)(r0 + q) * DM + 8 * lane; a[q][0] = *(const f32x4*)s; a[q][1] = *(const f32x4*)(s + 4); a[q][2] = *(const f32x4*)(s + 512); a[q][3] = *(const f32x4*)(s + 516); }
.LBB0_204:
	v_readlane_b32 s4, v237, 3
	s_nop 3
	s_and_b32 s4, s4, 7
.Lp0wg:
	s_cmp_eq_u32 s4, 0
	s_cbranch_scc1 .Lp0wg_done
	s_sleep 40
	s_sub_u32 s4, s4, 1
	s_branch .Lp0wg
